# speedup vs baseline: 1.0028x; 1.0014x over previous
_Z13gather_kernelPK15HIP_vector_typeIjLj2EEPKiPK6OvfRecPKDF16_PKfPDF16_:
	s_lshr_b32 s3, s2, 2
	s_and_b32 s3, s3, 0x3ffffffe
	s_and_b32 s4, s2, 1
	s_or_b32 s3, s3, s4
	s_cmpk_gt_u32 s3, 0x186
	s_cbranch_scc1 .LBB1_156
	s_load_dwordx4 s[8:11], s[0:1], 0x0
	s_load_dwordx2 s[64:65], s[0:1], 0x20
	s_movk_i32 s4, 0x80
	s_lshl_b32 s12, s3, 4
	s_addk_i32 s12, 0x800
	v_lshrrev_b32_e32 v2, 6, v0
	v_cmp_gt_u32_e64 s[4:5], s4, v0
	v_lshlrev_b32_e32 v1, 2, v0
	v_readfirstlane_b32 s62, v2
	s_and_saveexec_b64 s[6:7], s[4:5]
	v_mov_b32_e32 v2, 0
	ds_write_b32 v1, v2 offset:10832
	s_or_b64 exec, exec, s[6:7]
	s_waitcnt lgkmcnt(0)
	v_cmp_gt_u32_e64 s[6:7], 64, v0
	s_and_saveexec_b64 s[12:13], s[6:7]
	v_mov_b32_e32 v2, 0
	ds_write_b32 v1, v2 offset:11856
	s_or_b64 exec, exec, s[12:13]
	s_waitcnt lgkmcnt(0)
	s_mul_i32 s15, s3, 0x5000
	s_mul_hi_u32 s13, s3, 0x5000
	s_add_u32 s8, s8, s15
	s_addc_u32 s9, s9, s13
	v_lshlrev_b32_e32 v2, 3, v0
	v_mov_b32_e32 v3, 0
	v_lshl_add_u64 v[4:5], s[8:9], 0, v[2:3]
	s_movk_i32 s13, 0x1000
	s_barrier
	global_load_dwordx2 v[20:21], v2, s[8:9]
	global_load_dwordx2 v[18:19], v2, s[8:9] offset:2048
	v_add_co_u32_e32 v2, vcc, s13, v4
	s_movk_i32 s13, 0x2000
	s_nop 0
	v_addc_co_u32_e32 v3, vcc, 0, v5, vcc
	v_add_co_u32_e32 v6, vcc, s13, v4
	s_movk_i32 s13, 0x3000
	s_nop 0
	v_addc_co_u32_e32 v7, vcc, 0, v5, vcc
	v_add_co_u32_e32 v24, vcc, s13, v4
	v_or_b32_e32 v23, 0x400, v0
	s_nop 0
	v_addc_co_u32_e32 v25, vcc, 0, v5, vcc
	v_lshlrev_b32_e32 v8, 3, v23
	v_or_b32_e32 v22, 0x800, v0
	v_add_co_u32_e32 v26, vcc, 0x4000, v4
	global_load_dwordx2 v[16:17], v[2:3], off
	global_load_dwordx2 v[14:15], v[2:3], off offset:2048
	global_load_dwordx2 v[12:13], v8, s[8:9]
	global_load_dwordx2 v[10:11], v[6:7], off offset:2048
	v_lshlrev_b32_e32 v28, 3, v22
	v_addc_co_u32_e32 v27, vcc, 0, v5, vcc
	global_load_dwordx2 v[8:9], v[24:25], off
	global_load_dwordx2 v[6:7], v[24:25], off offset:2048
	global_load_dwordx2 v[4:5], v28, s[8:9]
	global_load_dwordx2 v[2:3], v[26:27], off offset:2048
	s_lshl_b32 s51, s3, 4
	s_addk_i32 s51, 0x800
	s_load_dwordx4 s[36:39], s[10:11], s51 offset:0x0
	s_load_dword s33, s[10:11], 0x640
	s_load_dword s63, s[64:65], 0x0
	v_mov_b32_e32 v54, 1
	s_waitcnt lgkmcnt(0)
	s_min_u32 s36, s36, 0x280
	s_min_u32 s37, s37, 0x280
	s_min_u32 s38, s38, 0x280
	s_min_u32 s39, s39, 0x280
	s_addk_i32 s37, 0x280
	s_addk_i32 s38, 0x500
	s_addk_i32 s39, 0x780
	s_cmp_ge_u32 s62, 2
	s_cselect_b32 s54, s37, s36
	s_cselect_b32 s59, s39, s38
	s_mov_b32 s52, s36
	s_mov_b32 s53, s36
	s_mov_b32 s55, s37
	s_mov_b32 s56, s37
	s_mov_b32 s57, s38
	s_mov_b32 s58, s38
	s_mov_b32 s60, s39
	s_mov_b32 s61, s39
	v_cmp_gt_i32_e32 vcc, s52, v0
	s_and_saveexec_b64 s[8:9], vcc
	s_waitcnt vmcnt(9)
	v_lshrrev_b32_e32 v33, 16, v20
	v_lshlrev_b32_e32 v53, 2, v33
	ds_add_rtn_u32 v43, v53, v54 offset:10832
	s_or_b64 exec, exec, s[8:9]
	v_or_b32_e32 v55, 0x100, v0
	v_cmp_gt_i32_e32 vcc, s53, v55
	s_and_saveexec_b64 s[8:9], vcc
	s_waitcnt vmcnt(8)
	v_lshrrev_b32_e32 v34, 16, v18
	v_lshlrev_b32_e32 v53, 2, v34
	ds_add_rtn_u32 v44, v53, v54 offset:10832
	s_or_b64 exec, exec, s[8:9]
	v_or_b32_e32 v55, 0x200, v0
	v_cmp_gt_i32_e32 vcc, s54, v55
	s_and_saveexec_b64 s[8:9], vcc
	s_waitcnt vmcnt(7)
	v_lshrrev_b32_e32 v35, 16, v16
	v_lshlrev_b32_e32 v53, 2, v35
	ds_add_rtn_u32 v45, v53, v54 offset:10832
	s_or_b64 exec, exec, s[8:9]
	v_or_b32_e32 v55, 0x300, v0
	v_cmp_gt_i32_e32 vcc, s55, v55
	s_and_saveexec_b64 s[8:9], vcc
	s_waitcnt vmcnt(6)
	v_lshrrev_b32_e32 v36, 16, v14
	v_lshlrev_b32_e32 v53, 2, v36
	ds_add_rtn_u32 v46, v53, v54 offset:10832
	s_or_b64 exec, exec, s[8:9]
	v_or_b32_e32 v55, 0x400, v0
	v_cmp_gt_i32_e32 vcc, s56, v55
	s_and_saveexec_b64 s[8:9], vcc
	s_waitcnt vmcnt(5)
	v_lshrrev_b32_e32 v37, 16, v12
	v_lshlrev_b32_e32 v53, 2, v37
	ds_add_rtn_u32 v47, v53, v54 offset:10832
	s_or_b64 exec, exec, s[8:9]
	v_or_b32_e32 v55, 0x500, v0
	v_cmp_gt_i32_e32 vcc, s57, v55
	s_and_saveexec_b64 s[8:9], vcc
	s_waitcnt vmcnt(4)
	v_lshrrev_b32_e32 v38, 16, v10
	v_lshlrev_b32_e32 v53, 2, v38
	ds_add_rtn_u32 v48, v53, v54 offset:10832
	s_or_b64 exec, exec, s[8:9]
	v_or_b32_e32 v55, 0x600, v0
	v_cmp_gt_i32_e32 vcc, s58, v55
	s_and_saveexec_b64 s[8:9], vcc
	s_waitcnt vmcnt(3)
	v_lshrrev_b32_e32 v39, 16, v8
	v_lshlrev_b32_e32 v53, 2, v39
	ds_add_rtn_u32 v49, v53, v54 offset:10832
	s_or_b64 exec, exec, s[8:9]
	v_or_b32_e32 v55, 0x700, v0
	v_cmp_gt_i32_e32 vcc, s59, v55
	s_and_saveexec_b64 s[8:9], vcc
	s_waitcnt vmcnt(2)
	v_lshrrev_b32_e32 v40, 16, v6
	v_lshlrev_b32_e32 v53, 2, v40
	ds_add_rtn_u32 v50, v53, v54 offset:10832
	s_or_b64 exec, exec, s[8:9]
	v_or_b32_e32 v55, 0x800, v0
	v_cmp_gt_i32_e32 vcc, s60, v55
	s_and_saveexec_b64 s[8:9], vcc
	s_waitcnt vmcnt(1)
	v_lshrrev_b32_e32 v41, 16, v4
	v_lshlrev_b32_e32 v53, 2, v41
	ds_add_rtn_u32 v51, v53, v54 offset:10832
	s_or_b64 exec, exec, s[8:9]
	v_or_b32_e32 v55, 0x900, v0
	v_cmp_gt_i32_e32 vcc, s61, v55
	s_and_saveexec_b64 s[8:9], vcc
	s_waitcnt vmcnt(0)
	v_lshrrev_b32_e32 v42, 16, v2
	v_lshlrev_b32_e32 v53, 2, v42
	ds_add_rtn_u32 v52, v53, v54 offset:10832
	s_or_b64 exec, exec, s[8:9]
	s_waitcnt lgkmcnt(0)
	v_cmp_gt_i32_e32 vcc, s52, v0
	v_lshl_or_b32 v56, v43, 8, v33
	s_nop 0
	v_cndmask_b32_e32 v32, -1, v56, vcc
	v_or_b32_e32 v55, 0x100, v0
	v_cmp_gt_i32_e32 vcc, s53, v55
	v_lshl_or_b32 v56, v44, 8, v34
	s_nop 0
	v_cndmask_b32_e32 v27, -1, v56, vcc
	v_or_b32_e32 v55, 0x200, v0
	v_cmp_gt_i32_e32 vcc, s54, v55
	v_lshl_or_b32 v56, v45, 8, v35
	s_nop 0
	v_cndmask_b32_e32 v31, -1, v56, vcc
	v_or_b32_e32 v55, 0x300, v0
	v_cmp_gt_i32_e32 vcc, s55, v55
	v_lshl_or_b32 v56, v46, 8, v36
	s_nop 0
	v_cndmask_b32_e32 v26, -1, v56, vcc
	v_or_b32_e32 v55, 0x400, v0
	v_cmp_gt_i32_e32 vcc, s56, v55
	v_lshl_or_b32 v56, v47, 8, v37
	s_nop 0
	v_cndmask_b32_e32 v30, -1, v56, vcc
	v_or_b32_e32 v55, 0x500, v0
	v_cmp_gt_i32_e32 vcc, s57, v55
	v_lshl_or_b32 v56, v48, 8, v38
	s_nop 0
	v_cndmask_b32_e32 v24, -1, v56, vcc
	v_or_b32_e32 v55, 0x600, v0
	v_cmp_gt_i32_e32 vcc, s58, v55
	v_lshl_or_b32 v56, v49, 8, v39
	s_nop 0
	v_cndmask_b32_e32 v29, -1, v56, vcc
	v_or_b32_e32 v55, 0x700, v0
	v_cmp_gt_i32_e32 vcc, s59, v55
	v_lshl_or_b32 v56, v50, 8, v40
	s_nop 0
	v_cndmask_b32_e32 v23, -1, v56, vcc
	v_or_b32_e32 v55, 0x800, v0
	v_cmp_gt_i32_e32 vcc, s60, v55
	v_lshl_or_b32 v56, v51, 8, v41
	s_nop 0
	v_cndmask_b32_e32 v28, -1, v56, vcc
	v_or_b32_e32 v55, 0x900, v0
	v_cmp_gt_i32_e32 vcc, s61, v55
	v_lshl_or_b32 v56, v52, 8, v42
	s_nop 0
	v_cndmask_b32_e32 v22, -1, v56, vcc

.LBB1_46:
	s_or_b64 exec, exec, s[0:1]
	v_lshrrev_b32_e32 v1, 3, v25
	v_lshrrev_b32_e32 v57, 6, v0
	v_lshlrev_b32_e32 v58, 2, v1
	s_waitcnt lgkmcnt(0)
	s_barrier
	v_lshlrev_b32_e32 v0, 4, v0
	v_lshl_or_b32 v59, v57, 5, v58
	s_bfe_u32 s0, s2, 0x20001
	v_and_b32_e32 v56, 0x70, v0
	ds_read_b32 v0, v59 offset:11344
	s_mul_i32 s1, s0, 0x61a800
	s_add_u32 s14, s14, s1
	s_addc_u32 s15, s15, 0
	s_and_b32 s21, s19, 0xffff
	s_lshl_b32 s34, s3, 7
	s_waitcnt lgkmcnt(0)
	s_cmp_gt_i32 s33, 0
	v_add_f32_e64 v40, s63, 1.0
	s_cselect_b64 s[16:17], -1, 0
	s_lshl_b32 s19, s0, 7
	v_add_u32_e32 v60, s34, v0
	s_mov_b32 s0, 0xc350
	s_mov_b32 s23, 0x20000
	s_mov_b32 s22, 0x186a000
	v_mov_b32_e32 v41, v40
	v_cmp_gt_i32_e32 vcc, s0, v60
	s_and_saveexec_b64 s[24:25], vcc
	s_cbranch_execz .LBB1_81
	v_lshl_or_b32 v1, v60, 7, v56
	global_load_dwordx4 v[4:7], v1, s[14:15]
	v_mov_b32_e32 v1, 0x2840
	v_lshl_add_u32 v0, v0, 2, v1
	ds_read2_b32 v[46:47], v0 offset1:1
	v_mov_b32_e32 v0, 0
	v_mov_b32_e32 v1, v0
	v_mov_b64_e32 v[44:45], v[0:1]
	v_mov_b64_e32 v[42:43], v[0:1]
	s_waitcnt lgkmcnt(0)
	v_cmp_lt_i32_e32 vcc, v46, v47
	s_waitcnt vmcnt(1)
	v_mov_b64_e32 v[2:3], v[0:1]
	s_and_saveexec_b64 s[26:27], vcc
	s_cbranch_execz .LBB1_75
	v_mov_b32_e32 v2, v0
	v_mov_b32_e32 v3, v0
	v_mov_b32_e32 v1, v0
	v_mov_b64_e32 v[10:11], v[2:3]
	v_mov_b64_e32 v[14:15], v[2:3]
	v_mov_b64_e32 v[18:19], v[2:3]
	v_mov_b64_e32 v[22:23], v[2:3]
	v_mov_b64_e32 v[26:27], v[2:3]
	v_mov_b64_e32 v[30:31], v[2:3]
	v_mov_b64_e32 v[34:35], v[2:3]
	v_lshlrev_b32_e32 v61, 2, v46
	v_add_u32_e32 v46, 7, v46
	s_mov_b64 s[28:29], 0
	s_mov_b32 s20, 0x7fff80
	v_mov_b64_e32 v[8:9], v[0:1]
	v_mov_b64_e32 v[12:13], v[0:1]
	v_mov_b64_e32 v[16:17], v[0:1]
	v_mov_b64_e32 v[20:21], v[0:1]
	v_mov_b64_e32 v[24:25], v[0:1]
	v_mov_b64_e32 v[28:29], v[0:1]
	v_mov_b64_e32 v[32:33], v[0:1]
	v_mov_b32_e32 v42, v0
	v_mov_b32_e32 v43, v0
	v_mov_b32_e32 v44, v0
	v_mov_b32_e32 v45, v0
	s_branch .LBB1_50

	.amdhsa_kernel _Z13gather_kernelPK15HIP_vector_typeIjLj2EEPKiPK6OvfRecPKDF16_PKfPDF16_
		.amdhsa_group_segment_fixed_size 12112
		.amdhsa_private_segment_fixed_size 0
		.amdhsa_kernarg_size 48
		.amdhsa_user_sgpr_count 2
		.amdhsa_user_sgpr_dispatch_ptr 0
		.amdhsa_user_sgpr_queue_ptr 0
		.amdhsa_user_sgpr_kernarg_segment_ptr 1
		.amdhsa_user_sgpr_dispatch_id 0
		.amdhsa_user_sgpr_kernarg_preload_length 0
		.amdhsa_user_sgpr_kernarg_preload_offset 0
		.amdhsa_user_sgpr_private_segment_size 0
		.amdhsa_uses_dynamic_stack 0
		.amdhsa_enable_private_segment 0
		.amdhsa_system_sgpr_workgroup_id_x 1
		.amdhsa_system_sgpr_workgroup_id_y 0
		.amdhsa_system_sgpr_workgroup_id_z 0
		.amdhsa_system_sgpr_workgroup_info 0
		.amdhsa_system_vgpr_workitem_id 0
		.amdhsa_next_free_vgpr 63
		.amdhsa_next_free_sgpr 66
		.amdhsa_accum_offset 64
		.amdhsa_reserve_vcc 1
		.amdhsa_float_round_mode_32 0
		.amdhsa_float_round_mode_16_64 0
		.amdhsa_float_denorm_mode_32 3
		.amdhsa_float_denorm_mode_16_64 3
		.amdhsa_dx10_clamp 1
		.amdhsa_ieee_mode 1
		.amdhsa_fp16_overflow 0
		.amdhsa_tg_split 0
		.amdhsa_exception_fp_ieee_invalid_op 0
		.amdhsa_exception_fp_denorm_src 0
		.amdhsa_exception_fp_ieee_div_zero 0
		.amdhsa_exception_fp_ieee_overflow 0
		.amdhsa_exception_fp_ieee_underflow 0
		.amdhsa_exception_fp_ieee_inexact 0
		.amdhsa_exception_int_div_zero 0
	.end_amdhsa_kernel
